# FFN up/down epilogues: v_permlane16_swap pairs, dwordx4 stores (half the store instructions); combine wait deferral; nt prologue stores
# speedup vs baseline: 1.0163x; 1.0158x over previous
.LBB0_762:
	s_andn2_b64 vcc, exec, s[6:7]
	s_cbranch_vccnz .LBB0_764
	v_lshl_add_u32 v2, s36, 8, v48
	s_waitcnt lgkmcnt(0)
	v_ashrrev_i32_e32 v3, 31, v2
	v_lshlrev_b64 v[4:5], 10, v[2:3]
	v_lshl_add_u64 v[2:3], v[2:3], 2, s[54:55]
	global_load_dword v7, v[2:3], off offset:704
	global_load_dword v6, v[2:3], off offset:640
	global_load_dword v8, v[2:3], off offset:576
	global_load_dword v9, v[2:3], off offset:512
	global_load_dword v10, v[2:3], off offset:192
	global_load_dword v11, v[2:3], off offset:128
	global_load_dword v12, v[2:3], off offset:64
	s_nop 0
	global_load_dword v2, v[2:3], off
	s_lshl_b32 s6, s44, 8
	s_ashr_i32 s7, s6, 31
	v_lshl_add_u64 v[4:5], s[50:51], 0, v[4:5]
	v_mov_b32_e32 v35, v67
	v_lshl_add_u64 v[4:5], v[4:5], 0, s[6:7]
	v_lshl_add_u64 v[4:5], v[4:5], 0, v[34:35]
	v_bfe_u32 v13, v238, 4, 1
	v_mul_u32_u24_e32 v13, 0x78, v13
	v_add_co_u32_e32 v4, vcc, v4, v13
	s_nop 1
	v_addc_co_u32_e32 v5, vcc, 0, v5, vcc
	s_waitcnt vmcnt(0)
	s_nop 0
	v_mul_f32_e32 v52, 0x42800000, v2
	v_mul_f32_e32 v54, 0x42800000, v12
	v_mul_f32_e32 v56, 0x42800000, v11
	v_mul_f32_e32 v58, 0x42800000, v10
	v_mul_f32_e32 v60, 0x42800000, v9
	v_mul_f32_e32 v62, 0x42800000, v8
	v_mul_f32_e32 v64, 0x42800000, v6
	v_mul_f32_e32 v16, 0x42800000, v7
	v_pk_mul_f32 v[36:37], v[72:73], v[52:53] op_sel_hi:[1,0]
	v_pk_mul_f32 v[38:39], v[74:75], v[52:53] op_sel_hi:[1,0]
	v_pk_mul_f32 v[40:41], v[192:193], v[52:53] op_sel_hi:[1,0]
	v_pk_mul_f32 v[42:43], v[194:195], v[52:53] op_sel_hi:[1,0]
	v_pk_mul_f32 v[44:45], v[164:165], v[52:53] op_sel_hi:[1,0]
	v_pk_mul_f32 v[46:47], v[166:167], v[52:53] op_sel_hi:[1,0]
	v_pk_mul_f32 v[48:49], v[160:161], v[52:53] op_sel_hi:[1,0]
	v_pk_mul_f32 v[50:51], v[162:163], v[52:53] op_sel_hi:[1,0]
	v_med3_f32 v36, v36, s19, v248
	v_med3_f32 v37, v37, s19, v248
	v_med3_f32 v38, v38, s19, v248
	v_med3_f32 v39, v39, s19, v248
	v_med3_f32 v40, v40, s19, v248
	v_med3_f32 v41, v41, s19, v248
	v_med3_f32 v42, v42, s19, v248
	v_med3_f32 v43, v43, s19, v248
	v_med3_f32 v44, v44, s19, v248
	v_med3_f32 v45, v45, s19, v248
	v_med3_f32 v46, v46, s19, v248
	v_med3_f32 v47, v47, s19, v248
	v_med3_f32 v48, v48, s19, v248
	v_med3_f32 v49, v49, s19, v248
	v_med3_f32 v50, v50, s19, v248
	v_med3_f32 v51, v51, s19, v248
	v_cvt_pk_fp8_f32 v20, v36, v37
	v_cvt_pk_fp8_f32 v21, v40, v41
	v_cvt_pk_fp8_f32 v22, v44, v45
	v_cvt_pk_fp8_f32 v23, v48, v49
	v_cvt_pk_fp8_f32 v20, v38, v39 op_sel:[0,0,1]
	v_cvt_pk_fp8_f32 v21, v42, v43 op_sel:[0,0,1]
	v_cvt_pk_fp8_f32 v22, v46, v47 op_sel:[0,0,1]
	v_cvt_pk_fp8_f32 v23, v50, v51 op_sel:[0,0,1]
	s_nop 1
	v_permlane16_swap_b32_e32 v20, v22
	v_permlane16_swap_b32_e32 v21, v23
	global_store_dwordx4 v[4:5], v[20:23], off
	v_pk_mul_f32 v[36:37], v[188:189], v[54:55] op_sel_hi:[1,0]
	v_pk_mul_f32 v[38:39], v[190:191], v[54:55] op_sel_hi:[1,0]
	v_pk_mul_f32 v[40:41], v[184:185], v[54:55] op_sel_hi:[1,0]
	v_pk_mul_f32 v[42:43], v[186:187], v[54:55] op_sel_hi:[1,0]
	v_pk_mul_f32 v[44:45], v[156:157], v[54:55] op_sel_hi:[1,0]
	v_pk_mul_f32 v[46:47], v[158:159], v[54:55] op_sel_hi:[1,0]
	v_pk_mul_f32 v[48:49], v[152:153], v[54:55] op_sel_hi:[1,0]
	v_pk_mul_f32 v[50:51], v[154:155], v[54:55] op_sel_hi:[1,0]
	v_med3_f32 v36, v36, s19, v248
	v_med3_f32 v37, v37, s19, v248
	v_med3_f32 v38, v38, s19, v248
	v_med3_f32 v39, v39, s19, v248
	v_med3_f32 v40, v40, s19, v248
	v_med3_f32 v41, v41, s19, v248
	v_med3_f32 v42, v42, s19, v248
	v_med3_f32 v43, v43, s19, v248
	v_med3_f32 v44, v44, s19, v248
	v_med3_f32 v45, v45, s19, v248
	v_med3_f32 v46, v46, s19, v248
	v_med3_f32 v47, v47, s19, v248
	v_med3_f32 v48, v48, s19, v248
	v_med3_f32 v49, v49, s19, v248
	v_med3_f32 v50, v50, s19, v248
	v_med3_f32 v51, v51, s19, v248
	v_cvt_pk_fp8_f32 v28, v36, v37
	v_cvt_pk_fp8_f32 v29, v40, v41
	v_cvt_pk_fp8_f32 v30, v44, v45
	v_cvt_pk_fp8_f32 v31, v48, v49
	v_cvt_pk_fp8_f32 v28, v38, v39 op_sel:[0,0,1]
	v_cvt_pk_fp8_f32 v29, v42, v43 op_sel:[0,0,1]
	v_cvt_pk_fp8_f32 v30, v46, v47 op_sel:[0,0,1]
	v_cvt_pk_fp8_f32 v31, v50, v51 op_sel:[0,0,1]
	v_add_co_u32_e32 v14, vcc, 0x4000, v4
	s_nop 1
	v_addc_co_u32_e32 v15, vcc, 0, v5, vcc
	v_permlane16_swap_b32_e32 v28, v30
	v_permlane16_swap_b32_e32 v29, v31
	global_store_dwordx4 v[14:15], v[28:31], off
	v_pk_mul_f32 v[36:37], v[180:181], v[56:57] op_sel_hi:[1,0]
	v_pk_mul_f32 v[38:39], v[182:183], v[56:57] op_sel_hi:[1,0]
	v_pk_mul_f32 v[40:41], v[176:177], v[56:57] op_sel_hi:[1,0]
	v_pk_mul_f32 v[42:43], v[178:179], v[56:57] op_sel_hi:[1,0]
	v_pk_mul_f32 v[44:45], v[148:149], v[56:57] op_sel_hi:[1,0]
	v_pk_mul_f32 v[46:47], v[150:151], v[56:57] op_sel_hi:[1,0]
	v_pk_mul_f32 v[48:49], v[144:145], v[56:57] op_sel_hi:[1,0]
	v_pk_mul_f32 v[50:51], v[146:147], v[56:57] op_sel_hi:[1,0]
	v_med3_f32 v36, v36, s19, v248
	v_med3_f32 v37, v37, s19, v248
	v_med3_f32 v38, v38, s19, v248
	v_med3_f32 v39, v39, s19, v248
	v_med3_f32 v40, v40, s19, v248
	v_med3_f32 v41, v41, s19, v248
	v_med3_f32 v42, v42, s19, v248
	v_med3_f32 v43, v43, s19, v248
	v_med3_f32 v44, v44, s19, v248
	v_med3_f32 v45, v45, s19, v248
	v_med3_f32 v46, v46, s19, v248
	v_med3_f32 v47, v47, s19, v248
	v_med3_f32 v48, v48, s19, v248
	v_med3_f32 v49, v49, s19, v248
	v_med3_f32 v50, v50, s19, v248
	v_med3_f32 v51, v51, s19, v248
	v_cvt_pk_fp8_f32 v20, v36, v37
	v_cvt_pk_fp8_f32 v21, v40, v41
	v_cvt_pk_fp8_f32 v22, v44, v45
	v_cvt_pk_fp8_f32 v23, v48, v49
	v_cvt_pk_fp8_f32 v20, v38, v39 op_sel:[0,0,1]
	v_cvt_pk_fp8_f32 v21, v42, v43 op_sel:[0,0,1]
	v_cvt_pk_fp8_f32 v22, v46, v47 op_sel:[0,0,1]
	v_cvt_pk_fp8_f32 v23, v50, v51 op_sel:[0,0,1]
	v_add_co_u32_e32 v14, vcc, 0x8000, v4
	s_nop 1
	v_addc_co_u32_e32 v15, vcc, 0, v5, vcc
	v_permlane16_swap_b32_e32 v20, v22
	v_permlane16_swap_b32_e32 v21, v23
	global_store_dwordx4 v[14:15], v[20:23], off
	v_pk_mul_f32 v[36:37], v[172:173], v[58:59] op_sel_hi:[1,0]
	v_pk_mul_f32 v[38:39], v[174:175], v[58:59] op_sel_hi:[1,0]
	v_pk_mul_f32 v[40:41], v[168:169], v[58:59] op_sel_hi:[1,0]
	v_pk_mul_f32 v[42:43], v[170:171], v[58:59] op_sel_hi:[1,0]
	v_pk_mul_f32 v[44:45], v[140:141], v[58:59] op_sel_hi:[1,0]
	v_pk_mul_f32 v[46:47], v[142:143], v[58:59] op_sel_hi:[1,0]
	v_pk_mul_f32 v[48:49], v[136:137], v[58:59] op_sel_hi:[1,0]
	v_pk_mul_f32 v[50:51], v[138:139], v[58:59] op_sel_hi:[1,0]
	v_med3_f32 v36, v36, s19, v248
	v_med3_f32 v37, v37, s19, v248
	v_med3_f32 v38, v38, s19, v248
	v_med3_f32 v39, v39, s19, v248
	v_med3_f32 v40, v40, s19, v248
	v_med3_f32 v41, v41, s19, v248
	v_med3_f32 v42, v42, s19, v248
	v_med3_f32 v43, v43, s19, v248
	v_med3_f32 v44, v44, s19, v248
	v_med3_f32 v45, v45, s19, v248
	v_med3_f32 v46, v46, s19, v248
	v_med3_f32 v47, v47, s19, v248
	v_med3_f32 v48, v48, s19, v248
	v_med3_f32 v49, v49, s19, v248
	v_med3_f32 v50, v50, s19, v248
	v_med3_f32 v51, v51, s19, v248
	v_cvt_pk_fp8_f32 v28, v36, v37
	v_cvt_pk_fp8_f32 v29, v40, v41
	v_cvt_pk_fp8_f32 v30, v44, v45
	v_cvt_pk_fp8_f32 v31, v48, v49
	v_cvt_pk_fp8_f32 v28, v38, v39 op_sel:[0,0,1]
	v_cvt_pk_fp8_f32 v29, v42, v43 op_sel:[0,0,1]
	v_cvt_pk_fp8_f32 v30, v46, v47 op_sel:[0,0,1]
	v_cvt_pk_fp8_f32 v31, v50, v51 op_sel:[0,0,1]
	v_add_co_u32_e32 v14, vcc, 0xc000, v4
	s_nop 1
	v_addc_co_u32_e32 v15, vcc, 0, v5, vcc
	v_permlane16_swap_b32_e32 v28, v30
	v_permlane16_swap_b32_e32 v29, v31
	global_store_dwordx4 v[14:15], v[28:31], off
	v_pk_mul_f32 v[36:37], v[132:133], v[60:61] op_sel_hi:[1,0]
	v_pk_mul_f32 v[38:39], v[134:135], v[60:61] op_sel_hi:[1,0]
	v_pk_mul_f32 v[40:41], v[128:129], v[60:61] op_sel_hi:[1,0]
	v_pk_mul_f32 v[42:43], v[130:131], v[60:61] op_sel_hi:[1,0]
	v_pk_mul_f32 v[44:45], v[100:101], v[60:61] op_sel_hi:[1,0]
	v_pk_mul_f32 v[46:47], v[102:103], v[60:61] op_sel_hi:[1,0]
	v_pk_mul_f32 v[48:49], v[96:97], v[60:61] op_sel_hi:[1,0]
	v_pk_mul_f32 v[50:51], v[98:99], v[60:61] op_sel_hi:[1,0]
	v_med3_f32 v36, v36, s19, v248
	v_med3_f32 v37, v37, s19, v248
	v_med3_f32 v38, v38, s19, v248
	v_med3_f32 v39, v39, s19, v248
	v_med3_f32 v40, v40, s19, v248
	v_med3_f32 v41, v41, s19, v248
	v_med3_f32 v42, v42, s19, v248
	v_med3_f32 v43, v43, s19, v248
	v_med3_f32 v44, v44, s19, v248
	v_med3_f32 v45, v45, s19, v248
	v_med3_f32 v46, v46, s19, v248
	v_med3_f32 v47, v47, s19, v248
	v_med3_f32 v48, v48, s19, v248
	v_med3_f32 v49, v49, s19, v248
	v_med3_f32 v50, v50, s19, v248
	v_med3_f32 v51, v51, s19, v248
	v_cvt_pk_fp8_f32 v20, v36, v37
	v_cvt_pk_fp8_f32 v21, v40, v41
	v_cvt_pk_fp8_f32 v22, v44, v45
	v_cvt_pk_fp8_f32 v23, v48, v49
	v_cvt_pk_fp8_f32 v20, v38, v39 op_sel:[0,0,1]
	v_cvt_pk_fp8_f32 v21, v42, v43 op_sel:[0,0,1]
	v_cvt_pk_fp8_f32 v22, v46, v47 op_sel:[0,0,1]
	v_cvt_pk_fp8_f32 v23, v50, v51 op_sel:[0,0,1]
	v_add_co_u32_e32 v14, vcc, 0x20000, v4
	s_nop 1
	v_addc_co_u32_e32 v15, vcc, 0, v5, vcc
	v_permlane16_swap_b32_e32 v20, v22
	v_permlane16_swap_b32_e32 v21, v23
	global_store_dwordx4 v[14:15], v[20:23], off
	v_pk_mul_f32 v[36:37], v[124:125], v[62:63] op_sel_hi:[1,0]
	v_pk_mul_f32 v[38:39], v[126:127], v[62:63] op_sel_hi:[1,0]
	v_pk_mul_f32 v[40:41], v[120:121], v[62:63] op_sel_hi:[1,0]
	v_pk_mul_f32 v[42:43], v[122:123], v[62:63] op_sel_hi:[1,0]
	v_pk_mul_f32 v[44:45], v[92:93], v[62:63] op_sel_hi:[1,0]
	v_pk_mul_f32 v[46:47], v[94:95], v[62:63] op_sel_hi:[1,0]
	v_pk_mul_f32 v[48:49], v[88:89], v[62:63] op_sel_hi:[1,0]
	v_pk_mul_f32 v[50:51], v[90:91], v[62:63] op_sel_hi:[1,0]
	v_med3_f32 v36, v36, s19, v248
	v_med3_f32 v37, v37, s19, v248
	v_med3_f32 v38, v38, s19, v248
	v_med3_f32 v39, v39, s19, v248
	v_med3_f32 v40, v40, s19, v248
	v_med3_f32 v41, v41, s19, v248
	v_med3_f32 v42, v42, s19, v248
	v_med3_f32 v43, v43, s19, v248
	v_med3_f32 v44, v44, s19, v248
	v_med3_f32 v45, v45, s19, v248
	v_med3_f32 v46, v46, s19, v248
	v_med3_f32 v47, v47, s19, v248
	v_med3_f32 v48, v48, s19, v248
	v_med3_f32 v49, v49, s19, v248
	v_med3_f32 v50, v50, s19, v248
	v_med3_f32 v51, v51, s19, v248
	v_cvt_pk_fp8_f32 v28, v36, v37
	v_cvt_pk_fp8_f32 v29, v40, v41
	v_cvt_pk_fp8_f32 v30, v44, v45
	v_cvt_pk_fp8_f32 v31, v48, v49
	v_cvt_pk_fp8_f32 v28, v38, v39 op_sel:[0,0,1]
	v_cvt_pk_fp8_f32 v29, v42, v43 op_sel:[0,0,1]
	v_cvt_pk_fp8_f32 v30, v46, v47 op_sel:[0,0,1]
	v_cvt_pk_fp8_f32 v31, v50, v51 op_sel:[0,0,1]
	v_add_co_u32_e32 v14, vcc, 0x24000, v4
	s_nop 1
	v_addc_co_u32_e32 v15, vcc, 0, v5, vcc
	v_permlane16_swap_b32_e32 v28, v30
	v_permlane16_swap_b32_e32 v29, v31
	global_store_dwordx4 v[14:15], v[28:31], off
	v_pk_mul_f32 v[36:37], v[116:117], v[64:65] op_sel_hi:[1,0]
	v_pk_mul_f32 v[38:39], v[118:119], v[64:65] op_sel_hi:[1,0]
	v_pk_mul_f32 v[40:41], v[112:113], v[64:65] op_sel_hi:[1,0]
	v_pk_mul_f32 v[42:43], v[114:115], v[64:65] op_sel_hi:[1,0]
	v_pk_mul_f32 v[44:45], v[84:85], v[64:65] op_sel_hi:[1,0]
	v_pk_mul_f32 v[46:47], v[86:87], v[64:65] op_sel_hi:[1,0]
	v_pk_mul_f32 v[48:49], v[80:81], v[64:65] op_sel_hi:[1,0]
	v_pk_mul_f32 v[50:51], v[82:83], v[64:65] op_sel_hi:[1,0]
	v_med3_f32 v36, v36, s19, v248
	v_med3_f32 v37, v37, s19, v248
	v_med3_f32 v38, v38, s19, v248
	v_med3_f32 v39, v39, s19, v248
	v_med3_f32 v40, v40, s19, v248
	v_med3_f32 v41, v41, s19, v248
	v_med3_f32 v42, v42, s19, v248
	v_med3_f32 v43, v43, s19, v248
	v_med3_f32 v44, v44, s19, v248
	v_med3_f32 v45, v45, s19, v248
	v_med3_f32 v46, v46, s19, v248
	v_med3_f32 v47, v47, s19, v248
	v_med3_f32 v48, v48, s19, v248
	v_med3_f32 v49, v49, s19, v248
	v_med3_f32 v50, v50, s19, v248
	v_med3_f32 v51, v51, s19, v248
	v_cvt_pk_fp8_f32 v20, v36, v37
	v_cvt_pk_fp8_f32 v21, v40, v41
	v_cvt_pk_fp8_f32 v22, v44, v45
	v_cvt_pk_fp8_f32 v23, v48, v49
	v_cvt_pk_fp8_f32 v20, v38, v39 op_sel:[0,0,1]
	v_cvt_pk_fp8_f32 v21, v42, v43 op_sel:[0,0,1]
	v_cvt_pk_fp8_f32 v22, v46, v47 op_sel:[0,0,1]
	v_cvt_pk_fp8_f32 v23, v50, v51 op_sel:[0,0,1]
	v_add_co_u32_e32 v14, vcc, 0x28000, v4
	s_nop 1
	v_addc_co_u32_e32 v15, vcc, 0, v5, vcc
	v_permlane16_swap_b32_e32 v20, v22
	v_permlane16_swap_b32_e32 v21, v23
	global_store_dwordx4 v[14:15], v[20:23], off
	v_pk_mul_f32 v[36:37], v[108:109], v[16:17] op_sel_hi:[1,0]
	v_pk_mul_f32 v[38:39], v[110:111], v[16:17] op_sel_hi:[1,0]
	v_pk_mul_f32 v[40:41], v[104:105], v[16:17] op_sel_hi:[1,0]
	v_pk_mul_f32 v[42:43], v[106:107], v[16:17] op_sel_hi:[1,0]
	v_pk_mul_f32 v[44:45], v[76:77], v[16:17] op_sel_hi:[1,0]
	v_pk_mul_f32 v[46:47], v[78:79], v[16:17] op_sel_hi:[1,0]
	v_pk_mul_f32 v[48:49], v[68:69], v[16:17] op_sel_hi:[1,0]
	v_pk_mul_f32 v[50:51], v[70:71], v[16:17] op_sel_hi:[1,0]
	v_med3_f32 v36, v36, s19, v248
	v_med3_f32 v37, v37, s19, v248
	v_med3_f32 v38, v38, s19, v248
	v_med3_f32 v39, v39, s19, v248
	v_med3_f32 v40, v40, s19, v248
	v_med3_f32 v41, v41, s19, v248
	v_med3_f32 v42, v42, s19, v248
	v_med3_f32 v43, v43, s19, v248
	v_med3_f32 v44, v44, s19, v248
	v_med3_f32 v45, v45, s19, v248
	v_med3_f32 v46, v46, s19, v248
	v_med3_f32 v47, v47, s19, v248
	v_med3_f32 v48, v48, s19, v248
	v_med3_f32 v49, v49, s19, v248
	v_med3_f32 v50, v50, s19, v248
	v_med3_f32 v51, v51, s19, v248
	v_cvt_pk_fp8_f32 v28, v36, v37
	v_cvt_pk_fp8_f32 v29, v40, v41
	v_cvt_pk_fp8_f32 v30, v44, v45
	v_cvt_pk_fp8_f32 v31, v48, v49
	v_cvt_pk_fp8_f32 v28, v38, v39 op_sel:[0,0,1]
	v_cvt_pk_fp8_f32 v29, v42, v43 op_sel:[0,0,1]
	v_cvt_pk_fp8_f32 v30, v46, v47 op_sel:[0,0,1]
	v_cvt_pk_fp8_f32 v31, v50, v51 op_sel:[0,0,1]
	v_add_co_u32_e32 v14, vcc, 0x2c000, v4
	s_nop 1
	v_addc_co_u32_e32 v15, vcc, 0, v5, vcc
	v_permlane16_swap_b32_e32 v28, v30
	v_permlane16_swap_b32_e32 v29, v31
	global_store_dwordx4 v[14:15], v[28:31], off

.LBB0_765:
	s_andn2_b64 vcc, exec, s[6:7]
	s_cbranch_vccnz .LBB0_768
	s_cmp_lg_u32 s1, 6
	s_cbranch_scc1 .LBB0_768
	v_exp_f32_e32 v8, v74
	v_exp_f32_e32 v9, v75
	v_pk_mul_f32 v[4:5], v[74:75], v[166:167]
	v_exp_f32_e32 v10, v194
	v_exp_f32_e32 v11, v195
	v_pk_add_f32 v[8:9], v[8:9], 1.0 op_sel_hi:[1,0]
	v_pk_mul_f32 v[6:7], v[72:73], v[164:165]
	v_rcp_f32_e32 v8, v8
	v_rcp_f32_e32 v9, v9
	v_pk_add_f32 v[10:11], v[10:11], 1.0 op_sel_hi:[1,0]
	v_lshl_add_u32 v2, s36, 8, v48
	v_rcp_f32_e32 v10, v10
	v_pk_mul_f32 v[4:5], v[8:9], v[4:5]
	v_rcp_f32_e32 v11, v11
	v_med3_f32 v8, v5, s19, v248
	v_med3_f32 v9, v4, s19, v248
	v_exp_f32_e32 v4, v72
	v_exp_f32_e32 v5, v73
	s_waitcnt lgkmcnt(0)
	v_ashrrev_i32_e32 v3, 31, v2
	v_lshlrev_b64 v[2:3], 11, v[2:3]
	s_lshl_b32 s6, s44, 7
	v_pk_add_f32 v[4:5], v[4:5], 1.0 op_sel_hi:[1,0]
	v_lshl_add_u64 v[2:3], s[50:51], 0, v[2:3]
	v_rcp_f32_e32 v4, v4
	v_rcp_f32_e32 v5, v5
	s_ashr_i32 s7, s6, 31
	v_lshl_add_u64 v[2:3], v[2:3], 0, s[6:7]
	v_mov_b32_e32 v35, v67
	v_pk_mul_f32 v[4:5], v[4:5], v[6:7]
	v_lshl_add_u64 v[2:3], v[2:3], 0, v[34:35]
	v_bfe_u32 v16, v238, 4, 1
	v_mul_u32_u24_e32 v16, 0x7ff8, v16
	v_add_co_u32_e32 v2, vcc, v2, v16
	s_nop 1
	v_addc_co_u32_e32 v3, vcc, 0, v3, vcc
	v_med3_f32 v5, v5, s19, v248
	v_med3_f32 v6, v4, s19, v248
	v_cvt_pk_fp8_f32 v12, v6, v5
	v_pk_mul_f32 v[6:7], v[194:195], v[162:163]
	v_pk_mul_f32 v[6:7], v[10:11], v[6:7]
	v_cvt_pk_fp8_f32 v12, v9, v8 op_sel:[0,0,1]
	v_med3_f32 v10, v6, s19, v248
	v_med3_f32 v11, v7, s19, v248
	v_exp_f32_e32 v6, v192
	v_exp_f32_e32 v7, v193
	v_pk_mul_f32 v[8:9], v[192:193], v[160:161]
	s_mov_b32 s6, 0x8000
	v_pk_add_f32 v[6:7], v[6:7], 1.0 op_sel_hi:[1,0]
	s_nop 0
	v_rcp_f32_e32 v6, v6
	v_rcp_f32_e32 v7, v7
	s_nop 0
	v_pk_mul_f32 v[6:7], v[6:7], v[8:9]
	s_nop 0
	v_med3_f32 v6, v6, s19, v248
	v_med3_f32 v7, v7, s19, v248
	v_cvt_pk_fp8_f32 v13, v6, v7
	v_exp_f32_e32 v8, v190
	v_exp_f32_e32 v9, v191
	v_pk_mul_f32 v[6:7], v[188:189], v[156:157]
	v_cvt_pk_fp8_f32 v13, v10, v11 op_sel:[0,0,1]
	v_exp_f32_e32 v10, v186
	v_pk_add_f32 v[8:9], v[8:9], 1.0 op_sel_hi:[1,0]
	v_exp_f32_e32 v11, v187
	v_rcp_f32_e32 v8, v8
	v_rcp_f32_e32 v9, v9
	v_pk_mul_f32 v[4:5], v[190:191], v[158:159]
	v_pk_add_f32 v[10:11], v[10:11], 1.0 op_sel_hi:[1,0]
	v_pk_mul_f32 v[4:5], v[8:9], v[4:5]
	v_rcp_f32_e32 v10, v10
	v_med3_f32 v8, v5, s19, v248
	v_med3_f32 v9, v4, s19, v248
	v_exp_f32_e32 v4, v188
	v_exp_f32_e32 v5, v189
	v_rcp_f32_e32 v11, v11
	v_pk_add_f32 v[4:5], v[4:5], 1.0 op_sel_hi:[1,0]
	s_nop 0
	v_rcp_f32_e32 v4, v4
	v_rcp_f32_e32 v5, v5
	s_nop 0
	v_pk_mul_f32 v[4:5], v[4:5], v[6:7]
	s_nop 0
	v_med3_f32 v5, v5, s19, v248
	v_med3_f32 v6, v4, s19, v248
	v_cvt_pk_fp8_f32 v14, v6, v5
	v_pk_mul_f32 v[6:7], v[186:187], v[154:155]
	v_pk_mul_f32 v[6:7], v[10:11], v[6:7]
	v_cvt_pk_fp8_f32 v14, v9, v8 op_sel:[0,0,1]
	v_med3_f32 v10, v6, s19, v248
	v_med3_f32 v11, v7, s19, v248
	v_exp_f32_e32 v6, v184
	v_exp_f32_e32 v7, v185
	v_pk_mul_f32 v[8:9], v[184:185], v[152:153]
	v_pk_add_f32 v[6:7], v[6:7], 1.0 op_sel_hi:[1,0]
	s_nop 0
	v_rcp_f32_e32 v6, v6
	v_rcp_f32_e32 v7, v7
	s_nop 0
	v_pk_mul_f32 v[6:7], v[6:7], v[8:9]
	s_nop 0
	v_med3_f32 v6, v6, s19, v248
	v_med3_f32 v7, v7, s19, v248
	v_cvt_pk_fp8_f32 v15, v6, v7
	v_exp_f32_e32 v8, v182
	v_exp_f32_e32 v9, v183
	v_add_co_u32_e32 v6, vcc, s6, v2
	v_cvt_pk_fp8_f32 v15, v10, v11 op_sel:[0,0,1]
	v_pk_add_f32 v[8:9], v[8:9], 1.0 op_sel_hi:[1,0]
	v_addc_co_u32_e32 v7, vcc, 0, v3, vcc
	v_rcp_f32_e32 v8, v8
	v_rcp_f32_e32 v9, v9
	v_subrev_co_u32_e32 v16, vcc, 0x8000, v6
	s_nop 1
	v_subbrev_co_u32_e32 v17, vcc, 0, v7, vcc
	v_permlane16_swap_b32_e32 v12, v14
	v_permlane16_swap_b32_e32 v13, v15
	global_store_dwordx4 v[16:17], v[12:15], off
	v_pk_mul_f32 v[4:5], v[182:183], v[150:151]
	v_exp_f32_e32 v10, v178
	v_pk_mul_f32 v[4:5], v[8:9], v[4:5]
	v_exp_f32_e32 v11, v179
	v_med3_f32 v8, v5, s19, v248
	v_med3_f32 v9, v4, s19, v248
	v_exp_f32_e32 v4, v180
	v_exp_f32_e32 v5, v181
	v_pk_add_f32 v[10:11], v[10:11], 1.0 op_sel_hi:[1,0]
	v_pk_mul_f32 v[6:7], v[180:181], v[148:149]
	v_rcp_f32_e32 v10, v10
	v_pk_add_f32 v[4:5], v[4:5], 1.0 op_sel_hi:[1,0]
	v_rcp_f32_e32 v11, v11
	v_rcp_f32_e32 v4, v4
	v_rcp_f32_e32 v5, v5
	s_mov_b32 s6, 0x10000
	v_pk_mul_f32 v[4:5], v[4:5], v[6:7]
	s_nop 0
	v_med3_f32 v5, v5, s19, v248
	v_med3_f32 v6, v4, s19, v248
	v_cvt_pk_fp8_f32 v12, v6, v5
	v_pk_mul_f32 v[6:7], v[178:179], v[146:147]
	v_pk_mul_f32 v[6:7], v[10:11], v[6:7]
	v_cvt_pk_fp8_f32 v12, v9, v8 op_sel:[0,0,1]
	v_med3_f32 v10, v6, s19, v248
	v_med3_f32 v11, v7, s19, v248
	v_exp_f32_e32 v6, v176
	v_exp_f32_e32 v7, v177
	v_pk_mul_f32 v[8:9], v[176:177], v[144:145]
	v_pk_add_f32 v[6:7], v[6:7], 1.0 op_sel_hi:[1,0]
	s_nop 0
	v_rcp_f32_e32 v6, v6
	v_rcp_f32_e32 v7, v7
	s_nop 0
	v_pk_mul_f32 v[6:7], v[6:7], v[8:9]
	s_nop 0
	v_med3_f32 v6, v6, s19, v248
	v_med3_f32 v7, v7, s19, v248
	v_cvt_pk_fp8_f32 v13, v6, v7
	v_exp_f32_e32 v8, v174
	v_exp_f32_e32 v9, v175
	v_add_co_u32_e32 v6, vcc, s6, v2
	v_cvt_pk_fp8_f32 v13, v10, v11 op_sel:[0,0,1]
	v_pk_add_f32 v[8:9], v[8:9], 1.0 op_sel_hi:[1,0]
	v_addc_co_u32_e32 v7, vcc, 0, v3, vcc
	v_rcp_f32_e32 v8, v8
	v_rcp_f32_e32 v9, v9
	v_pk_mul_f32 v[4:5], v[174:175], v[142:143]
	v_exp_f32_e32 v10, v170
	v_pk_mul_f32 v[4:5], v[8:9], v[4:5]
	v_exp_f32_e32 v11, v171
	v_med3_f32 v8, v5, s19, v248
	v_med3_f32 v9, v4, s19, v248
	v_exp_f32_e32 v4, v172
	v_exp_f32_e32 v5, v173
	v_pk_add_f32 v[10:11], v[10:11], 1.0 op_sel_hi:[1,0]
	v_pk_mul_f32 v[6:7], v[172:173], v[140:141]
	v_rcp_f32_e32 v10, v10
	v_pk_add_f32 v[4:5], v[4:5], 1.0 op_sel_hi:[1,0]
	v_rcp_f32_e32 v11, v11
	v_rcp_f32_e32 v4, v4
	v_rcp_f32_e32 v5, v5
	s_mov_b32 s6, 0x18000
	v_pk_mul_f32 v[4:5], v[4:5], v[6:7]
	s_nop 0
	v_med3_f32 v5, v5, s19, v248
	v_med3_f32 v6, v4, s19, v248
	v_cvt_pk_fp8_f32 v14, v6, v5
	v_pk_mul_f32 v[6:7], v[170:171], v[138:139]
	v_pk_mul_f32 v[6:7], v[10:11], v[6:7]
	v_cvt_pk_fp8_f32 v14, v9, v8 op_sel:[0,0,1]
	v_med3_f32 v10, v6, s19, v248
	v_med3_f32 v11, v7, s19, v248
	v_exp_f32_e32 v6, v168
	v_exp_f32_e32 v7, v169
	v_pk_mul_f32 v[8:9], v[168:169], v[136:137]
	v_pk_add_f32 v[6:7], v[6:7], 1.0 op_sel_hi:[1,0]
	s_nop 0
	v_rcp_f32_e32 v6, v6
	v_rcp_f32_e32 v7, v7
	s_nop 0
	v_pk_mul_f32 v[6:7], v[6:7], v[8:9]
	s_nop 0
	v_med3_f32 v6, v6, s19, v248
	v_med3_f32 v7, v7, s19, v248
	v_cvt_pk_fp8_f32 v15, v6, v7
	v_exp_f32_e32 v8, v134
	v_exp_f32_e32 v9, v135
	v_add_co_u32_e32 v6, vcc, s6, v2
	v_cvt_pk_fp8_f32 v15, v10, v11 op_sel:[0,0,1]
	v_pk_add_f32 v[8:9], v[8:9], 1.0 op_sel_hi:[1,0]
	v_addc_co_u32_e32 v7, vcc, 0, v3, vcc
	v_rcp_f32_e32 v8, v8
	v_rcp_f32_e32 v9, v9
	v_subrev_co_u32_e32 v16, vcc, 0x8000, v6
	s_nop 1
	v_subbrev_co_u32_e32 v17, vcc, 0, v7, vcc
	v_permlane16_swap_b32_e32 v12, v14
	v_permlane16_swap_b32_e32 v13, v15
	global_store_dwordx4 v[16:17], v[12:15], off
	v_pk_mul_f32 v[4:5], v[134:135], v[102:103]
	v_exp_f32_e32 v10, v130
	v_pk_mul_f32 v[4:5], v[8:9], v[4:5]
	v_exp_f32_e32 v11, v131
	v_med3_f32 v8, v5, s19, v248
	v_med3_f32 v9, v4, s19, v248
	v_exp_f32_e32 v4, v132
	v_exp_f32_e32 v5, v133
	v_pk_add_f32 v[10:11], v[10:11], 1.0 op_sel_hi:[1,0]
	v_pk_mul_f32 v[6:7], v[132:133], v[100:101]
	v_rcp_f32_e32 v10, v10
	v_pk_add_f32 v[4:5], v[4:5], 1.0 op_sel_hi:[1,0]
	v_rcp_f32_e32 v11, v11
	v_rcp_f32_e32 v4, v4
	v_rcp_f32_e32 v5, v5
	s_mov_b32 s6, 0x40000
	v_pk_mul_f32 v[4:5], v[4:5], v[6:7]
	s_nop 0
	v_med3_f32 v5, v5, s19, v248
	v_med3_f32 v6, v4, s19, v248
	v_cvt_pk_fp8_f32 v12, v6, v5
	v_pk_mul_f32 v[6:7], v[130:131], v[98:99]
	v_pk_mul_f32 v[6:7], v[10:11], v[6:7]
	v_cvt_pk_fp8_f32 v12, v9, v8 op_sel:[0,0,1]
	v_med3_f32 v10, v6, s19, v248
	v_med3_f32 v11, v7, s19, v248
	v_exp_f32_e32 v6, v128
	v_exp_f32_e32 v7, v129
	v_pk_mul_f32 v[8:9], v[128:129], v[96:97]
	v_pk_add_f32 v[6:7], v[6:7], 1.0 op_sel_hi:[1,0]
	s_nop 0
	v_rcp_f32_e32 v6, v6
	v_rcp_f32_e32 v7, v7
	s_nop 0
	v_pk_mul_f32 v[6:7], v[6:7], v[8:9]
	s_nop 0
	v_med3_f32 v6, v6, s19, v248
	v_med3_f32 v7, v7, s19, v248
	v_cvt_pk_fp8_f32 v13, v6, v7
	v_exp_f32_e32 v8, v126
	v_exp_f32_e32 v9, v127
	v_add_co_u32_e32 v6, vcc, s6, v2
	v_cvt_pk_fp8_f32 v13, v10, v11 op_sel:[0,0,1]
	v_pk_add_f32 v[8:9], v[8:9], 1.0 op_sel_hi:[1,0]
	v_addc_co_u32_e32 v7, vcc, 0, v3, vcc
	v_rcp_f32_e32 v8, v8
	v_rcp_f32_e32 v9, v9
	v_pk_mul_f32 v[4:5], v[126:127], v[94:95]
	v_exp_f32_e32 v10, v122
	v_pk_mul_f32 v[4:5], v[8:9], v[4:5]
	v_exp_f32_e32 v11, v123
	v_med3_f32 v8, v5, s19, v248
	v_med3_f32 v9, v4, s19, v248
	v_exp_f32_e32 v4, v124
	v_exp_f32_e32 v5, v125
	v_pk_add_f32 v[10:11], v[10:11], 1.0 op_sel_hi:[1,0]
	v_pk_mul_f32 v[6:7], v[124:125], v[92:93]
	v_rcp_f32_e32 v10, v10
	v_pk_add_f32 v[4:5], v[4:5], 1.0 op_sel_hi:[1,0]
	v_rcp_f32_e32 v11, v11
	v_rcp_f32_e32 v4, v4
	v_rcp_f32_e32 v5, v5
	s_mov_b32 s6, 0x48000
	v_pk_mul_f32 v[4:5], v[4:5], v[6:7]
	s_nop 0
	v_med3_f32 v5, v5, s19, v248
	v_med3_f32 v6, v4, s19, v248
	v_cvt_pk_fp8_f32 v14, v6, v5
	v_pk_mul_f32 v[6:7], v[122:123], v[90:91]
	v_pk_mul_f32 v[6:7], v[10:11], v[6:7]
	v_cvt_pk_fp8_f32 v14, v9, v8 op_sel:[0,0,1]
	v_med3_f32 v10, v6, s19, v248
	v_med3_f32 v11, v7, s19, v248
	v_exp_f32_e32 v6, v120
	v_exp_f32_e32 v7, v121
	v_pk_mul_f32 v[8:9], v[120:121], v[88:89]
	v_pk_add_f32 v[6:7], v[6:7], 1.0 op_sel_hi:[1,0]
	s_nop 0
	v_rcp_f32_e32 v6, v6
	v_rcp_f32_e32 v7, v7
	s_nop 0
	v_pk_mul_f32 v[6:7], v[6:7], v[8:9]
	s_nop 0
	v_med3_f32 v6, v6, s19, v248
	v_med3_f32 v7, v7, s19, v248
	v_cvt_pk_fp8_f32 v15, v6, v7
	v_exp_f32_e32 v8, v118
	v_exp_f32_e32 v9, v119
	v_add_co_u32_e32 v6, vcc, s6, v2
	v_cvt_pk_fp8_f32 v15, v10, v11 op_sel:[0,0,1]
	v_pk_add_f32 v[8:9], v[8:9], 1.0 op_sel_hi:[1,0]
	v_addc_co_u32_e32 v7, vcc, 0, v3, vcc
	v_rcp_f32_e32 v8, v8
	v_rcp_f32_e32 v9, v9
	v_subrev_co_u32_e32 v16, vcc, 0x8000, v6
	s_nop 1
	v_subbrev_co_u32_e32 v17, vcc, 0, v7, vcc
	v_permlane16_swap_b32_e32 v12, v14
	v_permlane16_swap_b32_e32 v13, v15
	global_store_dwordx4 v[16:17], v[12:15], off
	v_pk_mul_f32 v[4:5], v[118:119], v[86:87]
	v_exp_f32_e32 v10, v114
	v_pk_mul_f32 v[4:5], v[8:9], v[4:5]
	v_exp_f32_e32 v11, v115
	v_med3_f32 v8, v5, s19, v248
	v_med3_f32 v9, v4, s19, v248
	v_exp_f32_e32 v4, v116
	v_exp_f32_e32 v5, v117
	v_pk_add_f32 v[10:11], v[10:11], 1.0 op_sel_hi:[1,0]
	v_pk_mul_f32 v[6:7], v[116:117], v[84:85]
	v_rcp_f32_e32 v10, v10
	v_pk_add_f32 v[4:5], v[4:5], 1.0 op_sel_hi:[1,0]
	v_rcp_f32_e32 v11, v11
	v_rcp_f32_e32 v4, v4
	v_rcp_f32_e32 v5, v5
	s_mov_b32 s6, 0x50000
	v_pk_mul_f32 v[4:5], v[4:5], v[6:7]
	s_nop 0
	v_med3_f32 v5, v5, s19, v248
	v_med3_f32 v6, v4, s19, v248
	v_cvt_pk_fp8_f32 v12, v6, v5
	v_pk_mul_f32 v[6:7], v[114:115], v[82:83]
	v_pk_mul_f32 v[6:7], v[10:11], v[6:7]
	v_cvt_pk_fp8_f32 v12, v9, v8 op_sel:[0,0,1]
	v_med3_f32 v10, v6, s19, v248
	v_med3_f32 v11, v7, s19, v248
	v_exp_f32_e32 v6, v112
	v_exp_f32_e32 v7, v113
	v_pk_mul_f32 v[8:9], v[112:113], v[80:81]
	v_pk_add_f32 v[6:7], v[6:7], 1.0 op_sel_hi:[1,0]
	s_nop 0
	v_rcp_f32_e32 v6, v6
	v_rcp_f32_e32 v7, v7
	s_nop 0
	v_pk_mul_f32 v[6:7], v[6:7], v[8:9]
	s_nop 0
	v_med3_f32 v6, v6, s19, v248
	v_med3_f32 v7, v7, s19, v248
	v_cvt_pk_fp8_f32 v13, v6, v7
	v_exp_f32_e32 v8, v110
	v_exp_f32_e32 v9, v111
	v_add_co_u32_e32 v6, vcc, s6, v2
	v_cvt_pk_fp8_f32 v13, v10, v11 op_sel:[0,0,1]
	v_pk_add_f32 v[8:9], v[8:9], 1.0 op_sel_hi:[1,0]
	v_addc_co_u32_e32 v7, vcc, 0, v3, vcc
	v_rcp_f32_e32 v8, v8
	v_rcp_f32_e32 v9, v9
	v_pk_mul_f32 v[4:5], v[110:111], v[78:79]
	v_exp_f32_e32 v10, v106
	v_pk_mul_f32 v[4:5], v[8:9], v[4:5]
	v_exp_f32_e32 v11, v107
	v_med3_f32 v8, v5, s19, v248
	v_med3_f32 v9, v4, s19, v248
	v_exp_f32_e32 v4, v108
	v_exp_f32_e32 v5, v109
	v_pk_add_f32 v[10:11], v[10:11], 1.0 op_sel_hi:[1,0]
	v_pk_mul_f32 v[6:7], v[108:109], v[76:77]
	v_rcp_f32_e32 v10, v10
	v_pk_add_f32 v[4:5], v[4:5], 1.0 op_sel_hi:[1,0]
	v_rcp_f32_e32 v11, v11
	v_rcp_f32_e32 v4, v4
	v_rcp_f32_e32 v5, v5
	v_add_co_u32_e32 v2, vcc, 0x58000, v2
	v_pk_mul_f32 v[4:5], v[4:5], v[6:7]
	s_nop 0
	v_med3_f32 v5, v5, s19, v248
	v_med3_f32 v6, v4, s19, v248
	v_cvt_pk_fp8_f32 v14, v6, v5
	v_pk_mul_f32 v[6:7], v[106:107], v[70:71]
	v_pk_mul_f32 v[6:7], v[10:11], v[6:7]
	v_cvt_pk_fp8_f32 v14, v9, v8 op_sel:[0,0,1]
	v_med3_f32 v10, v6, s19, v248
	v_med3_f32 v11, v7, s19, v248
	v_exp_f32_e32 v6, v104
	v_exp_f32_e32 v7, v105
	v_pk_mul_f32 v[8:9], v[104:105], v[68:69]
	v_addc_co_u32_e32 v3, vcc, 0, v3, vcc
	v_pk_add_f32 v[6:7], v[6:7], 1.0 op_sel_hi:[1,0]
	s_nop 0
	v_rcp_f32_e32 v6, v6
	v_rcp_f32_e32 v7, v7
	s_nop 0
	v_pk_mul_f32 v[6:7], v[6:7], v[8:9]
	s_nop 0
	v_med3_f32 v6, v6, s19, v248
	v_med3_f32 v7, v7, s19, v248
	v_cvt_pk_fp8_f32 v15, v6, v7
	v_cvt_pk_fp8_f32 v15, v10, v11 op_sel:[0,0,1]
	v_subrev_co_u32_e32 v16, vcc, 0x8000, v2
	s_nop 1
	v_subbrev_co_u32_e32 v17, vcc, 0, v3, vcc
	v_permlane16_swap_b32_e32 v12, v14
	v_permlane16_swap_b32_e32 v13, v15
	global_store_dwordx4 v[16:17], v[12:15], off
